# U3f: tail-tile prefetch stacked on the store-ack wait removal
# baseline (speedup 1.0000x reference)
.Lu3_again:
	s_load_dword s3, s[0:1], 0x58
	v_lshrrev_b32_e32 v1, 6, v0
	s_waitcnt lgkmcnt(0)
	v_lshl_add_u32 v1, s2, 2, v1
	v_add_u32_e32 v1, s31, v1
	s_movk_i32 s2, 0xc35
	v_cmp_gt_i32_e32 vcc, s2, v1
	s_and_saveexec_b64 s[2:3], vcc
	s_cbranch_execz .LBB9_4
	s_load_dwordx4 s[4:7], s[0:1], 0x30
	s_load_dwordx2 s[2:3], s[0:1], 0x40
	s_load_dwordx4 s[8:11], s[0:1], 0x0
	v_and_b32_e32 v22, 31, v0
	v_lshlrev_b32_e32 v1, 5, v1
	v_or_b32_e32 v2, v1, v22
	v_ashrrev_i32_e32 v3, 31, v2
	v_lshlrev_b64 v[16:17], 7, v[2:3]
	v_and_b32_e32 v4, 32, v0
	s_waitcnt lgkmcnt(0)
	v_lshl_add_u64 v[2:3], s[10:11], 0, v[16:17]
	v_lshlrev_b32_e32 v28, 1, v4
	v_mov_b32_e32 v29, 0
	v_lshl_add_u64 v[18:19], v[2:3], 0, v[28:29]
	s_waitcnt vmcnt(0)
	v_mov_b32_e32 v2, v44
	v_mov_b32_e32 v3, v45
	v_mov_b32_e32 v4, v46
	v_mov_b32_e32 v5, v47
	v_mov_b32_e32 v6, v48
	v_mov_b32_e32 v7, v49
	v_mov_b32_e32 v8, v50
	v_mov_b32_e32 v9, v51
	v_mov_b32_e32 v12, v52
	v_mov_b32_e32 v13, v53
	v_mov_b32_e32 v14, v54
	v_mov_b32_e32 v15, v55
	v_mov_b32_e32 v24, v56
	v_mov_b32_e32 v25, v57
	v_mov_b32_e32 v26, v58
	v_mov_b32_e32 v27, v59
	v_lshl_add_u64 v[16:17], s[8:9], 0, v[16:17]
	v_lshl_add_u64 v[16:17], v[16:17], 0, v[28:29]
	v_and_b32_e32 v76, 0x80, v10
	v_and_b32_e32 v20, 63, v0
	v_lshrrev_b32_e32 v0, 3, v0
	v_and_or_b32 v0, v0, 4, v1
	v_ashrrev_i32_e32 v1, 31, v0
	s_waitcnt vmcnt(0)
	v_mov_b32_e32 v28, v60
	v_mov_b32_e32 v29, v61
	v_mov_b32_e32 v30, v62
	v_mov_b32_e32 v31, v63
	v_mov_b32_e32 v32, v64
	v_mov_b32_e32 v33, v65
	v_mov_b32_e32 v34, v66
	v_mov_b32_e32 v35, v67
	v_mov_b32_e32 v36, v68
	v_mov_b32_e32 v37, v69
	v_mov_b32_e32 v38, v70
	v_mov_b32_e32 v39, v71
	v_mov_b32_e32 v40, v72
	v_mov_b32_e32 v41, v73
	v_mov_b32_e32 v42, v74
	v_mov_b32_e32 v43, v75
	v_cvt_f32_f16_sdwa v17, v24 dst_sel:DWORD dst_unused:UNUSED_PAD src0_sel:WORD_1
	s_waitcnt vmcnt(0)
	v_lshlrev_b32_e32 v11, 16, v40
	v_and_b32_e32 v16, 0xffff0000, v40
	v_lshlrev_b32_e32 v21, 16, v41
	v_and_b32_e32 v23, 0xffff0000, v41
	v_lshlrev_b32_e32 v48, 16, v42
	v_and_b32_e32 v49, 0xffff0000, v42
	v_lshlrev_b32_e32 v50, 16, v43
	v_and_b32_e32 v51, 0xffff0000, v43
	v_lshlrev_b32_e32 v52, 16, v36
	v_and_b32_e32 v53, 0xffff0000, v36
	v_lshlrev_b32_e32 v54, 16, v37
	v_and_b32_e32 v55, 0xffff0000, v37
	v_lshlrev_b32_e32 v56, 16, v38
	v_and_b32_e32 v57, 0xffff0000, v38
	v_lshlrev_b32_e32 v58, 16, v39
	v_and_b32_e32 v59, 0xffff0000, v39
	v_lshlrev_b32_e32 v60, 16, v32
	v_and_b32_e32 v61, 0xffff0000, v32
	v_lshlrev_b32_e32 v62, 16, v33
	v_and_b32_e32 v63, 0xffff0000, v33
	v_lshlrev_b32_e32 v64, 16, v34
	v_and_b32_e32 v65, 0xffff0000, v34
	v_lshlrev_b32_e32 v66, 16, v35
	v_and_b32_e32 v67, 0xffff0000, v35
	v_lshlrev_b32_e32 v68, 16, v28
	v_and_b32_e32 v69, 0xffff0000, v28
	v_lshlrev_b32_e32 v70, 16, v29
	v_and_b32_e32 v71, 0xffff0000, v29
	v_lshlrev_b32_e32 v72, 16, v30
	v_and_b32_e32 v73, 0xffff0000, v30
	v_lshlrev_b32_e32 v74, 16, v31
	v_and_b32_e32 v75, 0xffff0000, v31
	ds_read_b128 v[28:31], v76 offset:32768
	ds_read_b128 v[32:35], v76 offset:32784
	ds_read_b128 v[36:39], v76 offset:32800
	ds_read_b128 v[40:43], v76 offset:32816
	ds_read_b128 v[44:47], v76 offset:33024
	s_waitcnt lgkmcnt(0)
	v_fma_f32 v10, v28, v11, v44
	v_fma_f32 v11, v29, v16, v45
	v_cvt_f32_f16_e32 v16, v24
	v_max_f32_e32 v10, 0, v10
	v_max_f32_e32 v11, 0, v11
	v_fmac_f32_e32 v47, v31, v23
	v_pk_add_f32 v[44:45], v[10:11], v[16:17]
	v_cvt_f32_f16_e32 v16, v25
	v_cvt_f32_f16_sdwa v17, v25 dst_sel:DWORD dst_unused:UNUSED_PAD src0_sel:WORD_1
	v_fma_f32 v10, v30, v21, v46
	ds_read_b128 v[28:31], v76 offset:33040
	v_max_f32_e32 v10, 0, v10
	v_max_f32_e32 v11, 0, v47
	v_pk_add_f32 v[46:47], v[10:11], v[16:17]
	v_cvt_f32_f16_e32 v16, v26
	v_cvt_f32_f16_sdwa v17, v26 dst_sel:DWORD dst_unused:UNUSED_PAD src0_sel:WORD_1
	s_waitcnt lgkmcnt(0)
	v_fma_f32 v10, v32, v48, v28
	v_fma_f32 v11, v33, v49, v29
	v_max_f32_e32 v10, 0, v10
	v_max_f32_e32 v11, 0, v11
	v_pk_add_f32 v[28:29], v[10:11], v[16:17]
	v_cvt_f32_f16_e32 v16, v27
	v_cvt_f32_f16_sdwa v17, v27 dst_sel:DWORD dst_unused:UNUSED_PAD src0_sel:WORD_1
	ds_read_b128 v[24:27], v76 offset:33056
	v_fma_f32 v10, v34, v50, v30
	v_fmac_f32_e32 v31, v35, v51
	v_max_f32_e32 v10, 0, v10
	v_max_f32_e32 v11, 0, v31
	v_pk_add_f32 v[30:31], v[10:11], v[16:17]
	v_cvt_f32_f16_e32 v16, v12
	v_cvt_f32_f16_sdwa v17, v12 dst_sel:DWORD dst_unused:UNUSED_PAD src0_sel:WORD_1
	s_waitcnt lgkmcnt(0)
	v_fma_f32 v10, v36, v52, v24
	v_fma_f32 v11, v37, v53, v25
	v_cvt_f32_f16_e32 v12, v13
	v_cvt_f32_f16_sdwa v13, v13 dst_sel:DWORD dst_unused:UNUSED_PAD src0_sel:WORD_1
	v_max_f32_e32 v10, 0, v10
	v_max_f32_e32 v11, 0, v11
	v_pk_add_f32 v[24:25], v[10:11], v[16:17]
	v_fma_f32 v10, v38, v54, v26
	v_fmac_f32_e32 v27, v39, v55
	v_max_f32_e32 v10, 0, v10
	v_max_f32_e32 v11, 0, v27
	v_pk_add_f32 v[26:27], v[10:11], v[12:13]
	ds_read_b128 v[10:13], v76 offset:33072
	v_cvt_f32_f16_e32 v16, v14
	v_cvt_f32_f16_sdwa v17, v14 dst_sel:DWORD dst_unused:UNUSED_PAD src0_sel:WORD_1
	v_lshlrev_b32_e32 v23, 4, v20
	s_waitcnt lgkmcnt(0)
	v_fma_f32 v10, v40, v56, v10
	v_fma_f32 v11, v41, v57, v11
	v_max_f32_e32 v10, 0, v10
	v_max_f32_e32 v11, 0, v11
	v_fmac_f32_e32 v13, v43, v59
	v_pk_add_f32 v[32:33], v[10:11], v[16:17]
	v_fma_f32 v10, v42, v58, v12
	v_max_f32_e32 v11, 0, v13
	v_cvt_f32_f16_e32 v12, v15
	v_cvt_f32_f16_sdwa v13, v15 dst_sel:DWORD dst_unused:UNUSED_PAD src0_sel:WORD_1
	v_max_f32_e32 v10, 0, v10
	v_pk_add_f32 v[34:35], v[10:11], v[12:13]
	ds_read_b128 v[10:13], v76 offset:32832
	ds_read_b128 v[14:17], v76 offset:33088
	s_waitcnt lgkmcnt(0)
	v_fma_f32 v10, v10, v60, v14
	v_fma_f32 v11, v11, v61, v15
	v_cvt_f32_f16_e32 v14, v6
	v_cvt_f32_f16_sdwa v15, v6 dst_sel:DWORD dst_unused:UNUSED_PAD src0_sel:WORD_1
	v_max_f32_e32 v10, 0, v10
	v_max_f32_e32 v11, 0, v11
	v_fma_f32 v6, v12, v62, v16
	v_pk_add_f32 v[36:37], v[10:11], v[14:15]
	v_max_f32_e32 v10, 0, v6
	v_cvt_f32_f16_e32 v6, v7
	v_cvt_f32_f16_sdwa v7, v7 dst_sel:DWORD dst_unused:UNUSED_PAD src0_sel:WORD_1
	v_fmac_f32_e32 v17, v13, v63
	v_max_f32_e32 v11, 0, v17
	v_pk_add_f32 v[38:39], v[10:11], v[6:7]
	ds_read_b128 v[10:13], v76 offset:32848
	ds_read_b128 v[14:17], v76 offset:33104
	s_waitcnt lgkmcnt(0)
	v_fma_f32 v6, v10, v64, v14
	v_fma_f32 v7, v11, v65, v15
	v_cvt_f32_f16_e32 v10, v8
	v_cvt_f32_f16_sdwa v11, v8 dst_sel:DWORD dst_unused:UNUSED_PAD src0_sel:WORD_1
	v_cvt_f32_f16_e32 v8, v9
	v_cvt_f32_f16_sdwa v9, v9 dst_sel:DWORD dst_unused:UNUSED_PAD src0_sel:WORD_1
	v_max_f32_e32 v6, 0, v6
	v_max_f32_e32 v7, 0, v7
	v_pk_add_f32 v[40:41], v[6:7], v[10:11]
	v_fma_f32 v6, v12, v66, v16
	v_fmac_f32_e32 v17, v13, v67
	v_max_f32_e32 v6, 0, v6
	v_max_f32_e32 v7, 0, v17
	v_pk_add_f32 v[42:43], v[6:7], v[8:9]
	ds_read_b128 v[6:9], v76 offset:32864
	ds_read_b128 v[10:13], v76 offset:33120
	v_cvt_pk_f16_f32 v14, v44, v45
	v_cvt_pk_f16_f32 v15, v46, v47
	v_cvt_pk_f16_f32 v16, v28, v29
	v_cvt_pk_f16_f32 v17, v30, v31
	s_waitcnt lgkmcnt(0)
	v_fma_f32 v6, v6, v68, v10
	v_fma_f32 v7, v7, v69, v11
	v_cvt_f32_f16_e32 v10, v2
	v_cvt_f32_f16_sdwa v11, v2 dst_sel:DWORD dst_unused:UNUSED_PAD src0_sel:WORD_1
	v_max_f32_e32 v6, 0, v6
	v_max_f32_e32 v7, 0, v7
	v_fma_f32 v2, v8, v70, v12
	v_pk_add_f32 v[48:49], v[6:7], v[10:11]
	v_max_f32_e32 v6, 0, v2
	v_cvt_f32_f16_e32 v2, v3
	v_cvt_f32_f16_sdwa v3, v3 dst_sel:DWORD dst_unused:UNUSED_PAD src0_sel:WORD_1
	v_fmac_f32_e32 v13, v9, v71
	v_max_f32_e32 v7, 0, v13
	v_pk_add_f32 v[50:51], v[6:7], v[2:3]
	ds_read_b128 v[6:9], v76 offset:32880
	ds_read_b128 v[10:13], v76 offset:33136
	global_store_dwordx4 v[18:19], v[14:17], off
	s_waitcnt lgkmcnt(0)
	v_fma_f32 v2, v6, v72, v10
	v_fma_f32 v3, v7, v73, v11
	v_cvt_f32_f16_e32 v6, v4
	v_cvt_f32_f16_sdwa v7, v4 dst_sel:DWORD dst_unused:UNUSED_PAD src0_sel:WORD_1
	v_cvt_f32_f16_e32 v4, v5
	v_cvt_f32_f16_sdwa v5, v5 dst_sel:DWORD dst_unused:UNUSED_PAD src0_sel:WORD_1
	v_max_f32_e32 v2, 0, v2
	v_max_f32_e32 v3, 0, v3
	v_pk_add_f32 v[52:53], v[2:3], v[6:7]
	v_fma_f32 v2, v8, v74, v12
	v_fmac_f32_e32 v13, v9, v75
	v_max_f32_e32 v2, 0, v2
	v_max_f32_e32 v3, 0, v13
	v_pk_add_f32 v[54:55], v[2:3], v[4:5]
	v_cvt_pk_f16_f32 v10, v24, v25
	v_cvt_pk_f16_f32 v11, v26, v27
	v_cvt_pk_f16_f32 v12, v32, v33
	v_cvt_pk_f16_f32 v13, v34, v35
	v_cvt_pk_f16_f32 v6, v36, v37
	v_cvt_pk_f16_f32 v7, v38, v39
	v_cvt_pk_f16_f32 v8, v40, v41
	v_cvt_pk_f16_f32 v9, v42, v43
	v_cvt_pk_f16_f32 v2, v48, v49
	v_cvt_pk_f16_f32 v3, v50, v51
	v_cvt_pk_f16_f32 v4, v52, v53
	v_cvt_pk_f16_f32 v5, v54, v55
	global_store_dwordx4 v[18:19], v[10:13], off offset:16
	global_store_dwordx4 v[18:19], v[6:9], off offset:32
	global_store_dwordx4 v[18:19], v[2:5], off offset:48
	ds_read_b128 v[18:21], v23
	ds_read_b128 v[24:27], v23 offset:8192
	ds_read_b128 v[28:31], v23 offset:4096
	ds_read_b128 v[32:35], v23 offset:12288
	s_cmp_lg_u32 s31, 0
	s_cbranch_scc1 .Lu3_nopf
	v_lshrrev_b32_e32 v78, 6, v77
	s_lshl_b32 s33, s30, 2
	v_readfirstlane_b32 s32, v78
	s_add_i32 s32, s32, s33
	s_cmp_ge_u32 s32, 53
	s_cbranch_scc1 .Lu3_nopf
	s_add_i32 s32, s32, 0xc00
	s_lshl_b32 s32, s32, 5
	v_and_b32_e32 v78, 31, v77
	v_or_b32_e32 v78, s32, v78
	v_lshlrev_b32_e32 v78, 7, v78
	v_and_b32_e32 v76, 32, v77
	v_lshl_add_u32 v78, v76, 1, v78
	global_load_dwordx4 v[44:47], v78, s[22:23] offset:48
	global_load_dwordx4 v[48:51], v78, s[22:23] offset:32
	global_load_dwordx4 v[52:55], v78, s[22:23] offset:16
	global_load_dwordx4 v[56:59], v78, s[22:23]
	global_load_dwordx4 v[60:63], v78, s[20:21] offset:48
	global_load_dwordx4 v[64:67], v78, s[20:21] offset:32
	global_load_dwordx4 v[68:71], v78, s[20:21] offset:16
	global_load_dwordx4 v[72:75], v78, s[20:21]
.Lu3_nopf:
	v_accvgpr_mov_b32 a16, a0
	v_accvgpr_mov_b32 a17, a0
	v_accvgpr_mov_b32 a18, a0
	v_accvgpr_mov_b32 a19, a0
	v_accvgpr_mov_b32 a20, a0
	v_accvgpr_mov_b32 a21, a0
	v_accvgpr_mov_b32 a22, a0
	v_accvgpr_mov_b32 a23, a0
	v_accvgpr_mov_b32 a24, a0
	v_accvgpr_mov_b32 a25, a0
	v_accvgpr_mov_b32 a26, a0
	v_accvgpr_mov_b32 a27, a0
	v_accvgpr_mov_b32 a28, a0
	v_accvgpr_mov_b32 a29, a0
	v_accvgpr_mov_b32 a30, a0
	v_accvgpr_mov_b32 a31, a0
	v_accvgpr_mov_b32 a0, a1
	v_accvgpr_mov_b32 a2, a1
	v_accvgpr_mov_b32 a3, a1
	v_accvgpr_mov_b32 a4, a1
	v_accvgpr_mov_b32 a5, a1
	v_accvgpr_mov_b32 a6, a1
	v_accvgpr_mov_b32 a7, a1
	v_accvgpr_mov_b32 a8, a1
	v_accvgpr_mov_b32 a9, a1
	v_accvgpr_mov_b32 a10, a1
	v_accvgpr_mov_b32 a11, a1
	v_accvgpr_mov_b32 a12, a1
	v_accvgpr_mov_b32 a13, a1
	v_accvgpr_mov_b32 a14, a1
	v_accvgpr_mov_b32 a15, a1
	s_waitcnt lgkmcnt(3)
	v_mfma_f32_32x32x16_f16 a[16:31], v[14:17], v[18:21], a[16:31]
	s_waitcnt lgkmcnt(1)
	v_mfma_f32_32x32x16_f16 a[0:15], v[14:17], v[28:31], a[0:15]
	v_mfma_f32_32x32x16_f16 a[16:31], v[14:17], v[24:27], a[16:31]
	s_waitcnt lgkmcnt(0)
	v_mfma_f32_32x32x16_f16 a[0:15], v[14:17], v[32:35], a[0:15]
	ds_read_b128 v[18:21], v23 offset:1024
	ds_read_b128 v[24:27], v23 offset:9216
	ds_read_b128 v[28:31], v23 offset:5120
	ds_read_b128 v[32:35], v23 offset:13312
	s_waitcnt lgkmcnt(3)
	v_mfma_f32_32x32x16_f16 a[16:31], v[10:13], v[18:21], a[16:31]
	s_waitcnt lgkmcnt(1)
	v_mfma_f32_32x32x16_f16 a[0:15], v[10:13], v[28:31], a[0:15]
	v_mfma_f32_32x32x16_f16 a[16:31], v[10:13], v[24:27], a[16:31]
	s_waitcnt lgkmcnt(0)
	v_mfma_f32_32x32x16_f16 a[0:15], v[10:13], v[32:35], a[0:15]
	ds_read_b128 v[18:21], v23 offset:2048
	ds_read_b128 v[24:27], v23 offset:10240
	ds_read_b128 v[28:31], v23 offset:6144
	ds_read_b128 v[32:35], v23 offset:14336
	s_waitcnt lgkmcnt(3)
	v_mfma_f32_32x32x16_f16 a[16:31], v[6:9], v[18:21], a[16:31]
	s_waitcnt lgkmcnt(1)
	v_mfma_f32_32x32x16_f16 a[0:15], v[6:9], v[28:31], a[0:15]
	v_mfma_f32_32x32x16_f16 a[16:31], v[6:9], v[24:27], a[16:31]
	s_waitcnt lgkmcnt(0)
	v_mfma_f32_32x32x16_f16 a[0:15], v[6:9], v[32:35], a[0:15]
	ds_read_b128 v[18:21], v23 offset:3072
	ds_read_b128 v[24:27], v23 offset:11264
	ds_read_b128 v[28:31], v23 offset:7168
	ds_read_b128 v[32:35], v23 offset:15360
	s_waitcnt lgkmcnt(3)
	v_mfma_f32_32x32x16_f16 a[16:31], v[2:5], v[18:21], a[16:31]
	s_waitcnt lgkmcnt(1)
	v_mfma_f32_32x32x16_f16 a[0:15], v[2:5], v[28:31], a[0:15]
	v_mfma_f32_32x32x16_f16 a[16:31], v[2:5], v[24:27], a[16:31]
	s_waitcnt lgkmcnt(0)
	v_mfma_f32_32x32x16_f16 a[0:15], v[2:5], v[32:35], a[0:15]
	ds_read_b128 v[18:21], v23 offset:16384
	ds_read_b128 v[24:27], v23 offset:24576
	ds_read_b128 v[28:31], v23 offset:20480
	ds_read_b128 v[32:35], v23 offset:28672
	s_waitcnt lgkmcnt(3)
	v_mfma_f32_32x32x16_f16 a[32:47], v[14:17], v[18:21], 0
	s_waitcnt lgkmcnt(1)
	v_mfma_f32_32x32x16_f16 a[48:63], v[14:17], v[28:31], 0
	v_mfma_f32_32x32x16_f16 a[32:47], v[14:17], v[24:27], a[32:47]
	s_waitcnt lgkmcnt(0)
	v_mfma_f32_32x32x16_f16 a[48:63], v[14:17], v[32:35], a[48:63]
	ds_read_b128 v[14:17], v23 offset:17408
	ds_read_b128 v[18:21], v23 offset:25600
	ds_read_b128 v[24:27], v23 offset:21504
	ds_read_b128 v[28:31], v23 offset:29696
	s_waitcnt lgkmcnt(3)
	v_mfma_f32_32x32x16_f16 a[32:47], v[10:13], v[14:17], a[32:47]
	s_waitcnt lgkmcnt(1)
	v_mfma_f32_32x32x16_f16 a[48:63], v[10:13], v[24:27], a[48:63]
	v_mfma_f32_32x32x16_f16 a[32:47], v[10:13], v[18:21], a[32:47]
	s_waitcnt lgkmcnt(0)
	v_mfma_f32_32x32x16_f16 a[48:63], v[10:13], v[28:31], a[48:63]
	ds_read_b128 v[10:13], v23 offset:18432
	ds_read_b128 v[14:17], v23 offset:26624
	ds_read_b128 v[18:21], v23 offset:22528
	ds_read_b128 v[24:27], v23 offset:30720
	s_waitcnt lgkmcnt(3)
	v_mfma_f32_32x32x16_f16 a[32:47], v[6:9], v[10:13], a[32:47]
	s_waitcnt lgkmcnt(1)
	v_mfma_f32_32x32x16_f16 a[48:63], v[6:9], v[18:21], a[48:63]
	v_mfma_f32_32x32x16_f16 a[32:47], v[6:9], v[14:17], a[32:47]
	s_waitcnt lgkmcnt(0)
	v_mfma_f32_32x32x16_f16 a[48:63], v[6:9], v[24:27], a[48:63]
	ds_read_b128 v[10:13], v23 offset:19456
	ds_read_b128 v[6:9], v23 offset:27648
	ds_read_b128 v[18:21], v23 offset:23552
	ds_read_b128 v[14:17], v23 offset:31744
	s_waitcnt lgkmcnt(3)
	v_mfma_f32_32x32x16_f16 a[32:47], v[2:5], v[10:13], a[32:47]
	s_waitcnt lgkmcnt(1)
	v_mfma_f32_32x32x16_f16 a[48:63], v[2:5], v[18:21], a[48:63]
	v_mfma_f32_32x32x16_f16 a[32:47], v[2:5], v[6:9], a[32:47]
	v_lshlrev_b32_e32 v7, 2, v22
	s_waitcnt lgkmcnt(0)
	v_mfma_f32_32x32x16_f16 a[48:63], v[2:5], v[14:17], a[48:63]
	v_accvgpr_read_b32 v2, a0
	v_accvgpr_read_b32 v3, a16
	v_cvt_pk_bf16_f32 v6, v3, v2
	v_lshlrev_b64 v[2:3], 7, v[0:1]
	v_or_b32_e32 v2, v2, v7
	v_lshl_add_u64 v[4:5], s[6:7], 0, v[2:3]
	global_store_dword v[4:5], v6, off
	s_nop 1
	v_accvgpr_read_b32 v4, a32
	v_lshl_add_u64 v[2:3], s[2:3], 0, v[2:3]
	s_nop 0
	v_accvgpr_read_b32 v1, a48
	v_cvt_pk_bf16_f32 v1, v4, v1
	global_store_dword v[2:3], v1, off
	v_or_b32_e32 v2, 1, v0
	v_ashrrev_i32_e32 v3, 31, v2
	v_lshlrev_b64 v[2:3], 7, v[2:3]
	v_accvgpr_read_b32 v1, a1
	v_accvgpr_read_b32 v4, a17
	v_or_b32_e32 v2, v2, v7
	v_cvt_pk_bf16_f32 v1, v4, v1
	v_lshl_add_u64 v[4:5], s[6:7], 0, v[2:3]
	global_store_dword v[4:5], v1, off
	v_accvgpr_read_b32 v1, a49
	v_accvgpr_read_b32 v4, a33
	v_cvt_pk_bf16_f32 v1, v4, v1
	v_lshl_add_u64 v[2:3], s[2:3], 0, v[2:3]
	global_store_dword v[2:3], v1, off
	v_or_b32_e32 v2, 2, v0
	v_ashrrev_i32_e32 v3, 31, v2
	v_lshlrev_b64 v[2:3], 7, v[2:3]
	v_accvgpr_read_b32 v1, a2
	v_accvgpr_read_b32 v4, a18
	v_or_b32_e32 v2, v2, v7
	v_cvt_pk_bf16_f32 v1, v4, v1
	v_lshl_add_u64 v[4:5], s[6:7], 0, v[2:3]
	global_store_dword v[4:5], v1, off
	v_accvgpr_read_b32 v1, a50
	v_accvgpr_read_b32 v4, a34
	v_cvt_pk_bf16_f32 v1, v4, v1
	v_lshl_add_u64 v[2:3], s[2:3], 0, v[2:3]
	global_store_dword v[2:3], v1, off
	v_or_b32_e32 v2, 3, v0
	v_ashrrev_i32_e32 v3, 31, v2
	v_lshlrev_b64 v[2:3], 7, v[2:3]
	v_accvgpr_read_b32 v1, a3
	v_accvgpr_read_b32 v4, a19
	v_or_b32_e32 v2, v2, v7
	v_cvt_pk_bf16_f32 v1, v4, v1
	v_lshl_add_u64 v[4:5], s[6:7], 0, v[2:3]
	global_store_dword v[4:5], v1, off
	v_accvgpr_read_b32 v1, a51
	v_accvgpr_read_b32 v4, a35
	v_cvt_pk_bf16_f32 v1, v4, v1
	v_lshl_add_u64 v[2:3], s[2:3], 0, v[2:3]
	global_store_dword v[2:3], v1, off
	v_or_b32_e32 v2, 8, v0
	v_ashrrev_i32_e32 v3, 31, v2
	v_lshlrev_b64 v[2:3], 7, v[2:3]
	v_accvgpr_read_b32 v1, a4
	v_accvgpr_read_b32 v4, a20
	v_or_b32_e32 v2, v2, v7
	v_cvt_pk_bf16_f32 v1, v4, v1
	v_lshl_add_u64 v[4:5], s[6:7], 0, v[2:3]
	global_store_dword v[4:5], v1, off
	v_accvgpr_read_b32 v1, a52
	v_accvgpr_read_b32 v4, a36
	v_cvt_pk_bf16_f32 v1, v4, v1
	v_lshl_add_u64 v[2:3], s[2:3], 0, v[2:3]
	global_store_dword v[2:3], v1, off
	v_or_b32_e32 v2, 9, v0
	v_ashrrev_i32_e32 v3, 31, v2
	v_lshlrev_b64 v[2:3], 7, v[2:3]
	v_accvgpr_read_b32 v1, a5
	v_accvgpr_read_b32 v4, a21
	v_or_b32_e32 v2, v2, v7
	v_cvt_pk_bf16_f32 v1, v4, v1
	v_lshl_add_u64 v[4:5], s[6:7], 0, v[2:3]
	global_store_dword v[4:5], v1, off
	v_accvgpr_read_b32 v1, a53
	v_accvgpr_read_b32 v4, a37
	v_cvt_pk_bf16_f32 v1, v4, v1
	v_lshl_add_u64 v[2:3], s[2:3], 0, v[2:3]
	global_store_dword v[2:3], v1, off
	v_or_b32_e32 v2, 10, v0
	v_ashrrev_i32_e32 v3, 31, v2
	v_lshlrev_b64 v[2:3], 7, v[2:3]
	v_accvgpr_read_b32 v1, a6
	v_accvgpr_read_b32 v4, a22
	v_or_b32_e32 v2, v2, v7
	v_cvt_pk_bf16_f32 v1, v4, v1
	v_lshl_add_u64 v[4:5], s[6:7], 0, v[2:3]
	global_store_dword v[4:5], v1, off
	v_accvgpr_read_b32 v1, a54
	v_accvgpr_read_b32 v4, a38
	v_cvt_pk_bf16_f32 v1, v4, v1
	v_lshl_add_u64 v[2:3], s[2:3], 0, v[2:3]
	global_store_dword v[2:3], v1, off
	v_or_b32_e32 v2, 11, v0
	v_ashrrev_i32_e32 v3, 31, v2
	v_lshlrev_b64 v[2:3], 7, v[2:3]
	v_accvgpr_read_b32 v1, a7
	v_accvgpr_read_b32 v4, a23
	v_or_b32_e32 v2, v2, v7
	v_cvt_pk_bf16_f32 v1, v4, v1
	v_lshl_add_u64 v[4:5], s[6:7], 0, v[2:3]
	global_store_dword v[4:5], v1, off
	v_accvgpr_read_b32 v1, a55
	v_accvgpr_read_b32 v4, a39
	v_cvt_pk_bf16_f32 v1, v4, v1
	v_lshl_add_u64 v[2:3], s[2:3], 0, v[2:3]
	global_store_dword v[2:3], v1, off
	v_or_b32_e32 v2, 16, v0
	v_ashrrev_i32_e32 v3, 31, v2
	v_lshlrev_b64 v[2:3], 7, v[2:3]
	v_accvgpr_read_b32 v1, a8
	v_accvgpr_read_b32 v4, a24
	v_or_b32_e32 v2, v2, v7
	v_cvt_pk_bf16_f32 v1, v4, v1
	v_lshl_add_u64 v[4:5], s[6:7], 0, v[2:3]
	global_store_dword v[4:5], v1, off
	v_accvgpr_read_b32 v1, a56
	v_accvgpr_read_b32 v4, a40
	v_cvt_pk_bf16_f32 v1, v4, v1
	v_lshl_add_u64 v[2:3], s[2:3], 0, v[2:3]
	global_store_dword v[2:3], v1, off
	v_or_b32_e32 v2, 17, v0
	v_ashrrev_i32_e32 v3, 31, v2
	v_lshlrev_b64 v[2:3], 7, v[2:3]
	v_accvgpr_read_b32 v1, a9
	v_accvgpr_read_b32 v4, a25
	v_or_b32_e32 v2, v2, v7
	v_cvt_pk_bf16_f32 v1, v4, v1
	v_lshl_add_u64 v[4:5], s[6:7], 0, v[2:3]
	global_store_dword v[4:5], v1, off
	v_accvgpr_read_b32 v1, a57
	v_accvgpr_read_b32 v4, a41
	v_cvt_pk_bf16_f32 v1, v4, v1
	v_lshl_add_u64 v[2:3], s[2:3], 0, v[2:3]
	global_store_dword v[2:3], v1, off
	v_or_b32_e32 v2, 18, v0
	v_ashrrev_i32_e32 v3, 31, v2
	v_lshlrev_b64 v[2:3], 7, v[2:3]
	v_accvgpr_read_b32 v1, a10
	v_accvgpr_read_b32 v4, a26
	v_or_b32_e32 v2, v2, v7
	v_cvt_pk_bf16_f32 v1, v4, v1
	v_lshl_add_u64 v[4:5], s[6:7], 0, v[2:3]
	global_store_dword v[4:5], v1, off
	v_accvgpr_read_b32 v1, a58
	v_accvgpr_read_b32 v4, a42
	v_cvt_pk_bf16_f32 v1, v4, v1
	v_lshl_add_u64 v[2:3], s[2:3], 0, v[2:3]
	global_store_dword v[2:3], v1, off
	v_or_b32_e32 v2, 19, v0
	v_ashrrev_i32_e32 v3, 31, v2
	v_lshlrev_b64 v[2:3], 7, v[2:3]
	v_accvgpr_read_b32 v1, a11
	v_accvgpr_read_b32 v4, a27
	v_or_b32_e32 v2, v2, v7
	v_cvt_pk_bf16_f32 v1, v4, v1
	v_lshl_add_u64 v[4:5], s[6:7], 0, v[2:3]
	global_store_dword v[4:5], v1, off
	v_accvgpr_read_b32 v1, a59
	v_accvgpr_read_b32 v4, a43
	v_cvt_pk_bf16_f32 v1, v4, v1
	v_lshl_add_u64 v[2:3], s[2:3], 0, v[2:3]
	global_store_dword v[2:3], v1, off
	v_or_b32_e32 v2, 24, v0
	v_ashrrev_i32_e32 v3, 31, v2
	v_lshlrev_b64 v[2:3], 7, v[2:3]
	v_accvgpr_read_b32 v1, a12
	v_accvgpr_read_b32 v4, a28
	v_or_b32_e32 v2, v2, v7
	v_cvt_pk_bf16_f32 v1, v4, v1
	v_lshl_add_u64 v[4:5], s[6:7], 0, v[2:3]
	global_store_dword v[4:5], v1, off
	v_accvgpr_read_b32 v1, a60
	v_accvgpr_read_b32 v4, a44
	v_cvt_pk_bf16_f32 v1, v4, v1
	v_lshl_add_u64 v[2:3], s[2:3], 0, v[2:3]
	global_store_dword v[2:3], v1, off
	v_or_b32_e32 v2, 25, v0
	v_ashrrev_i32_e32 v3, 31, v2
	v_lshlrev_b64 v[2:3], 7, v[2:3]
	v_accvgpr_read_b32 v1, a13
	v_accvgpr_read_b32 v4, a29
	v_or_b32_e32 v2, v2, v7
	v_cvt_pk_bf16_f32 v1, v4, v1
	v_lshl_add_u64 v[4:5], s[6:7], 0, v[2:3]
	global_store_dword v[4:5], v1, off
	v_accvgpr_read_b32 v1, a61
	v_accvgpr_read_b32 v4, a45
	v_cvt_pk_bf16_f32 v1, v4, v1
	v_lshl_add_u64 v[2:3], s[2:3], 0, v[2:3]
	global_store_dword v[2:3], v1, off
	v_or_b32_e32 v2, 26, v0
	v_ashrrev_i32_e32 v3, 31, v2
	v_lshlrev_b64 v[2:3], 7, v[2:3]
	v_accvgpr_read_b32 v1, a14
	v_accvgpr_read_b32 v4, a30
	v_or_b32_e32 v2, v2, v7
	v_cvt_pk_bf16_f32 v1, v4, v1
	v_lshl_add_u64 v[4:5], s[6:7], 0, v[2:3]
	global_store_dword v[4:5], v1, off
	v_accvgpr_read_b32 v1, a62
	v_accvgpr_read_b32 v4, a46
	v_cvt_pk_bf16_f32 v1, v4, v1
	v_lshl_add_u64 v[2:3], s[2:3], 0, v[2:3]
	v_or_b32_e32 v0, 27, v0
	global_store_dword v[2:3], v1, off
	v_ashrrev_i32_e32 v1, 31, v0
	v_lshlrev_b64 v[0:1], 7, v[0:1]
	v_accvgpr_read_b32 v2, a15
	v_accvgpr_read_b32 v3, a31
	v_or_b32_e32 v0, v0, v7
	v_cvt_pk_bf16_f32 v4, v3, v2
	v_lshl_add_u64 v[2:3], s[6:7], 0, v[0:1]
	global_store_dword v[2:3], v4, off
	v_accvgpr_read_b32 v2, a63
	v_accvgpr_read_b32 v3, a47
	v_cvt_pk_bf16_f32 v2, v3, v2
	v_lshl_add_u64 v[0:1], s[2:3], 0, v[0:1]
	global_store_dword v[0:1], v2, off
	s_cmp_lg_u32 s31, 0
	s_cbranch_scc1 .LBB9_4
	s_mov_b64 exec, -1
	v_lshrrev_b32_e32 v78, 6, v77
	s_lshl_b32 s33, s30, 2
	v_readfirstlane_b32 s32, v78
	s_add_i32 s32, s32, s33
	s_cmp_ge_u32 s32, 53
	s_cbranch_scc1 .LBB9_4
	s_movk_i32 s31, 0xc00
	s_mov_b32 s2, s30
	v_mov_b32_e32 v0, v77
	v_mov_b32_e32 v10, v79
	v_and_b32_e32 v1, 31, v0
	v_lshlrev_b32_e32 v1, 3, v1
	global_load_dwordx2 a[0:1], v1, s[24:25]
	s_waitcnt vmcnt(0)
	s_branch .Lu3_again
